# output-wave loop head: s_part read address computed before the barrier (3 fewer post-barrier instructions), on top of loop-edge rotation
# baseline (speedup 1.0000x reference)
.LBB0_85:
	s_waitcnt vmcnt(3)
	v_mov_b32_e32 v167, 0
	s_and_b64 vcc, exec, s[0:1]
	s_cbranch_vccz .LBB0_107
	s_lshl_b32 s0, s33, 2
	s_and_b32 s0, s0, 12
	v_bfe_u32 v192, v0, 3, 2
	s_waitcnt vmcnt(0)
	v_or3_b32 v172, v192, s0, v182
	v_and_b32_e32 v170, 7, v0
	s_setprio 2
	v_mov_b32_e32 v222, 0
	v_mov_b32_e32 v223, 0
	ds_read_b128 v[162:165], v179
	ds_read_b128 v[166:169], v179 offset:32
	ds_read_b128 v[174:177], v179 offset:64
	ds_read_b128 v[188:191], v179 offset:96
	s_movk_i32 s16, 0xffc0
	s_mov_b32 s25, 0x7f61b1e6
	s_waitcnt lgkmcnt(0)
	v_mfma_f32_32x32x16_f16 v[66:81], v[98:101], v[162:165], v[2:17]
	s_lshl_b32 s1, s33, 4
	s_add_i32 s1, s1, 0x1a000
	s_mov_b32 s4, 0x1a000
	v_cmp_eq_u32_e32 vcc, 0, v170
	s_mov_b32 s17, 1
	v_add_u32_e32 v179, 0x1200, v179
	s_mov_b32 s26, 0x3d3851ec
	v_mfma_f32_32x32x16_f16 v[66:81], v[102:105], v[166:169], v[66:81]
	s_movk_i32 s27, 0x3ff
	s_movk_i32 s28, 0x3ff0
	v_mfma_f32_32x32x16_f16 v[66:81], v[106:109], v[174:177], v[66:81]
	v_mfma_f32_32x32x16_f16 v[66:81], v[110:113], v[188:191], v[66:81]
	s_nop 11
	v_and_b32_e32 v82, 0xffffffc0, v66
	v_and_or_b32 v83, v67, s16, 1
	v_and_or_b32 v84, v68, s16, 2
	v_and_or_b32 v85, v69, s16, 3
	v_and_or_b32 v86, v70, s16, 4
	v_and_or_b32 v87, v71, s16, 5
	v_and_or_b32 v88, v72, s16, 6
	v_and_or_b32 v89, v73, s16, 7
	v_and_or_b32 v90, v74, s16, 8
	v_and_or_b32 v91, v75, s16, 9
	v_and_or_b32 v92, v76, s16, 10
	v_and_or_b32 v93, v77, s16, 11
	v_and_or_b32 v94, v78, s16, 12
	v_and_or_b32 v95, v79, s16, 13
	v_and_or_b32 v96, v80, s16, 14
	v_and_or_b32 v97, v81, s16, 15
	v_mfma_f32_32x32x16_f16 v[66:81], v[114:117], v[162:165], v[18:33]
	v_med3_f32 v171, v82, v83, s25
	v_min3_f32 v82, v82, s25, v83
	v_med3_f32 v83, v82, v84, v85
	v_min3_f32 v82, v82, v84, v85
	v_med3_f32 v84, v82, v86, v87
	v_min3_f32 v82, v82, v86, v87
	v_min3_f32 v83, v171, s25, v83
	v_mfma_f32_32x32x16_f16 v[66:81], v[118:121], v[166:169], v[66:81]
	v_med3_f32 v85, v82, v88, v89
	v_min3_f32 v82, v82, v88, v89
	v_min3_f32 v83, v83, v84, v85
	v_med3_f32 v84, v82, v90, v91
	v_min3_f32 v82, v82, v90, v91
	v_med3_f32 v85, v82, v92, v93
	v_min3_f32 v82, v82, v92, v93
	v_mfma_f32_32x32x16_f16 v[66:81], v[122:125], v[174:177], v[66:81]
	v_min3_f32 v83, v83, v84, v85
	v_med3_f32 v84, v82, v94, v95
	v_min3_f32 v82, v82, v94, v95
	v_med3_f32 v85, v82, v96, v97
	v_min3_f32 v171, v82, v96, v97
	v_min3_f32 v173, v83, v84, v85
	v_mfma_f32_32x32x16_f16 v[66:81], v[126:129], v[188:191], v[66:81]
	v_mfma_f32_32x32x16_f16 v[82:97], v[130:133], v[162:165], v[34:49]
	s_nop 10
	v_and_or_b32 v66, v66, s16, 16
	v_and_or_b32 v67, v67, s16, 17
	v_and_or_b32 v68, v68, s16, 18
	v_and_or_b32 v69, v69, s16, 19
	v_med3_f32 v187, v171, v66, v67
	v_min3_f32 v66, v171, v66, v67
	v_and_or_b32 v70, v70, s16, 20
	v_and_or_b32 v71, v71, s16, 21
	v_med3_f32 v67, v66, v68, v69
	v_min3_f32 v66, v66, v68, v69
	v_and_or_b32 v72, v72, s16, 22
	v_and_or_b32 v73, v73, s16, 23
	v_med3_f32 v68, v66, v70, v71
	v_min3_f32 v66, v66, v70, v71
	v_and_or_b32 v74, v74, s16, 24
	v_and_or_b32 v75, v75, s16, 25
	v_min3_f32 v67, v173, v187, v67
	v_med3_f32 v69, v66, v72, v73
	v_min3_f32 v66, v66, v72, v73
	v_and_or_b32 v76, v76, s16, 26
	v_and_or_b32 v77, v77, s16, 27
	v_min3_f32 v67, v67, v68, v69
	v_med3_f32 v68, v66, v74, v75
	v_min3_f32 v66, v66, v74, v75
	v_and_or_b32 v78, v78, s16, 28
	v_and_or_b32 v79, v79, s16, 29
	v_med3_f32 v69, v66, v76, v77
	v_min3_f32 v66, v66, v76, v77
	v_and_or_b32 v80, v80, s16, 30
	v_and_or_b32 v81, v81, s16, 31
	v_min3_f32 v67, v67, v68, v69
	v_med3_f32 v68, v66, v78, v79
	v_min3_f32 v66, v66, v78, v79
	v_med3_f32 v69, v66, v80, v81
	v_mfma_f32_32x32x16_f16 v[82:97], v[134:137], v[166:169], v[82:97]
	v_min3_f32 v171, v66, v80, v81
	v_min3_f32 v173, v67, v68, v69
	v_mfma_f32_32x32x16_f16 v[66:81], v[146:149], v[162:165], v[50:65]
	v_mfma_f32_32x32x16_f16 v[82:97], v[138:141], v[174:177], v[82:97]
	v_mfma_f32_32x32x16_f16 v[66:81], v[150:153], v[166:169], v[66:81]
	v_mov_b32_e32 v167, 0
	v_mfma_f32_32x32x16_f16 v[82:97], v[142:145], v[188:191], v[82:97]
	v_mfma_f32_32x32x16_f16 v[66:81], v[154:157], v[174:177], v[66:81]
	s_nop 10
	v_and_or_b32 v82, v82, s16, 32
	v_and_or_b32 v83, v83, s16, 33
	v_and_or_b32 v84, v84, s16, 34
	v_and_or_b32 v85, v85, s16, 35
	v_med3_f32 v162, v171, v82, v83
	v_min3_f32 v82, v171, v82, v83
	v_and_or_b32 v86, v86, s16, 36
	v_mfma_f32_32x32x16_f16 v[66:81], v[158:161], v[188:191], v[66:81]
	v_and_or_b32 v87, v87, s16, 37
	v_med3_f32 v83, v82, v84, v85
	v_min3_f32 v82, v82, v84, v85
	v_and_or_b32 v88, v88, s16, 38
	v_and_or_b32 v89, v89, s16, 39
	v_med3_f32 v84, v82, v86, v87
	v_min3_f32 v82, v82, v86, v87
	v_and_or_b32 v90, v90, s16, 40
	v_and_or_b32 v91, v91, s16, 41
	v_min3_f32 v83, v173, v162, v83
	v_med3_f32 v85, v82, v88, v89
	v_min3_f32 v82, v82, v88, v89
	v_and_or_b32 v92, v92, s16, 42
	v_and_or_b32 v93, v93, s16, 43
	v_min3_f32 v83, v83, v84, v85
	v_med3_f32 v84, v82, v90, v91
	v_min3_f32 v82, v82, v90, v91
	v_and_or_b32 v94, v94, s16, 44
	v_and_or_b32 v95, v95, s16, 45
	v_med3_f32 v85, v82, v92, v93
	v_min3_f32 v82, v82, v92, v93
	v_and_or_b32 v96, v96, s16, 46
	v_and_or_b32 v97, v97, s16, 47
	v_min3_f32 v83, v83, v84, v85
	v_med3_f32 v84, v82, v94, v95
	v_min3_f32 v82, v82, v94, v95
	v_med3_f32 v85, v82, v96, v97
	v_min3_f32 v82, v82, v96, v97
	v_and_or_b32 v66, v66, s16, 48
	v_and_or_b32 v67, v67, s16, 49
	v_min3_f32 v83, v83, v84, v85
	v_and_or_b32 v68, v68, s16, 50
	v_and_or_b32 v69, v69, s16, 51
	v_med3_f32 v84, v82, v66, v67
	v_min3_f32 v66, v82, v66, v67
	v_and_or_b32 v70, v70, s16, 52
	v_and_or_b32 v71, v71, s16, 53
	v_med3_f32 v67, v66, v68, v69
	v_min3_f32 v66, v66, v68, v69
	v_and_or_b32 v72, v72, s16, 54
	v_and_or_b32 v73, v73, s16, 55
	v_med3_f32 v68, v66, v70, v71
	v_min3_f32 v66, v66, v70, v71
	v_and_or_b32 v74, v74, s16, 56
	v_and_or_b32 v75, v75, s16, 57
	v_min3_f32 v67, v83, v84, v67
	v_med3_f32 v69, v66, v72, v73
	v_min3_f32 v66, v66, v72, v73
	v_and_or_b32 v76, v76, s16, 58
	v_and_or_b32 v77, v77, s16, 59
	v_min3_f32 v67, v67, v68, v69
	v_med3_f32 v68, v66, v74, v75
	v_min3_f32 v66, v66, v74, v75
	v_and_or_b32 v78, v78, s16, 60
	v_and_or_b32 v79, v79, s16, 61
	v_med3_f32 v69, v66, v76, v77
	v_min3_f32 v66, v66, v76, v77
	v_and_or_b32 v80, v80, s16, 62
	v_or_b32_e32 v81, 63, v81
	v_min3_f32 v67, v67, v68, v69
	v_med3_f32 v68, v66, v78, v79
	v_min3_f32 v66, v66, v78, v79
	v_med3_f32 v69, v66, v80, v81
	v_min3_f32 v67, v67, v68, v69
	v_lshlrev_b32_e32 v68, 3, v184
	v_min3_f32 v66, v66, v80, v81
	v_add3_u32 v177, s1, v185, v68
	ds_write_b64 v177, v[66:67]
	v_mul_u32_u24_e32 v66, 0x90, v172
	v_lshlrev_b32_e32 v67, 4, v170
	v_add3_u32 v185, v67, v66, s4
	v_and_b32_e32 v66, 0xff, v0
	v_mov_b32_e32 v67, 0x12000
	v_or_b32_e32 v173, 16, v183
	s_mov_b32 s1, 0x12000
	v_lshl_or_b32 v175, v66, 4, v67
	v_lshlrev_b32_e32 v66, 8, v173
	v_or3_b32 v174, v66, v178, s1
	s_lshl_b32 s1, s2, 17
	v_or3_b32 v166, s1, v186, v178
	s_waitcnt lgkmcnt(0)
	s_barrier
	v_lshl_add_u64 v[168:169], s[12:13], 0, v[166:167]
	v_or_b32_e32 v166, 0x1000, v166
	v_lshlrev_b32_e32 v176, 7, v170
	v_lshl_add_u64 v[170:171], s[12:13], 0, v[166:167]
	v_add3_u32 v166, v182, s0, v192
	v_mov_b32_e32 v66, 0x20c00
	v_or_b32_e32 v187, 4, v176
	v_lshlrev_b32_e32 v188, 2, v183
	v_lshl_or_b32 v186, v166, 2, v66
	v_mov_b32_e32 v189, 0x21d44
	s_mov_b64 s[4:5], 0x2000
	v_bfrev_b32_e32 v190, 1
	v_mov_b32_e32 v254, v185
.LBB0_88:
	ds_read_b128 v[250:253], v254
	s_add_i32 s29, s17, -1
	ds_read_b128 v[194:197], v179
	ds_read_b128 v[198:201], v179 offset:32
	ds_read_b128 v[202:205], v179 offset:64
	ds_read_b128 v[206:209], v179 offset:96
	s_cmp_lt_u32 s17, 2
	s_cbranch_scc1 .Low_noout
	v_cmp_lt_i32_e64 s[0:1], -1, v192
	s_waitcnt vmcnt(0)
	s_and_saveexec_b64 s[6:7], s[0:1]
	s_cbranch_execz .Low_a_donel
	v_pk_add_f32 v[66:67], v[246:247], v[224:225] neg_lo:[0,1] neg_hi:[0,1]
	v_pk_add_f32 v[74:75], v[248:249], v[226:227] neg_lo:[0,1] neg_hi:[0,1]
	v_pk_fma_f32 v[222:223], v[66:67], v[66:67], v[222:223]
	v_pk_fma_f32 v[222:223], v[74:75], v[74:75], v[222:223]
	v_pk_add_f32 v[66:67], v[224:225], v[66:67]
	v_pk_add_f32 v[68:69], v[226:227], v[74:75]
	global_store_dwordx4 v[168:169], v[66:69], off sc0 sc1
	s_nop 1

.Low_m_done:
	s_or_b64 exec, exec, s[6:7]
	s_waitcnt lgkmcnt(1)
	v_mfma_f32_32x32x16_f16 v[66:81], v[98:101], v[194:197], v[2:17]
	v_mfma_f32_32x32x16_f16 v[66:81], v[102:105], v[198:201], v[66:81]
	v_add_u32_e32 v254, 0x20c00, v188
	s_waitcnt lgkmcnt(0)
	ds_read_b32 v191, v254 offset:64
	ds_read_b32 v192, v254
	v_mfma_f32_32x32x16_f16 v[66:81], v[106:109], v[202:205], v[66:81]
	v_mfma_f32_32x32x16_f16 v[66:81], v[110:113], v[206:209], v[66:81]
	v_mfma_f32_32x32x16_f16 v[82:97], v[114:117], v[194:197], v[18:33]
	s_waitcnt lgkmcnt(0)
	v_and_b32_e32 v212, s27, v191
	v_lshl_or_b32 v212, v212, 8, v178
	global_load_dwordx4 v[162:165], v212, s[22:23]
	v_and_b32_e32 v213, s27, v192
	v_lshl_or_b32 v213, v213, 8, v178
	global_load_dwordx4 v[246:249], v213, s[22:23]
	s_and_b32 s1, s29, 3
	v_lshl_add_u32 v212, s1, 13, v175
	v_lshl_add_u32 v213, s1, 13, v174
	ds_read_b128 v[224:227], v212
	ds_read_b128 v[228:231], v213
	v_and_b32_e32 v66, 0xffffffc0, v66
	v_and_or_b32 v67, v67, s16, 1
	v_and_or_b32 v68, v68, s16, 2
	v_and_or_b32 v69, v69, s16, 3
	v_med3_f32 v211, v66, v67, s25
	v_and_or_b32 v70, v70, s16, 4
	v_min3_f32 v210, v66, s25, v67
	v_and_or_b32 v71, v71, s16, 5
	v_mfma_f32_32x32x16_f16 v[82:97], v[118:121], v[198:201], v[82:97]
	v_med3_f32 v214, v210, v68, v69
	v_and_or_b32 v72, v72, s16, 6
	v_min3_f32 v212, v210, v68, v69
	v_and_or_b32 v73, v73, s16, 7
	v_min3_f32 v213, v211, s25, v214
	v_med3_f32 v211, v212, v70, v71
	v_and_or_b32 v74, v74, s16, 8
	v_min3_f32 v210, v212, v70, v71
	v_mfma_f32_32x32x16_f16 v[82:97], v[122:125], v[202:205], v[82:97]
	v_and_or_b32 v75, v75, s16, 9
	v_med3_f32 v214, v210, v72, v73
	v_and_or_b32 v76, v76, s16, 10
	v_min3_f32 v212, v210, v72, v73
	v_and_or_b32 v77, v77, s16, 11
	v_min3_f32 v213, v213, v211, v214
	v_med3_f32 v211, v212, v74, v75
	v_and_or_b32 v78, v78, s16, 12
	v_mfma_f32_32x32x16_f16 v[82:97], v[126:129], v[206:209], v[82:97]
	v_min3_f32 v210, v212, v74, v75
	v_and_or_b32 v79, v79, s16, 13
	v_med3_f32 v214, v210, v76, v77
	v_and_or_b32 v80, v80, s16, 14
	v_min3_f32 v212, v210, v76, v77
	v_and_or_b32 v81, v81, s16, 15
	v_min3_f32 v213, v213, v211, v214
	v_med3_f32 v211, v212, v78, v79
	v_min3_f32 v210, v212, v78, v79
	v_med3_f32 v214, v210, v80, v81
	v_min3_f32 v212, v210, v80, v81
	v_min3_f32 v213, v213, v211, v214
	v_mfma_f32_32x32x16_f16 v[66:81], v[130:133], v[194:197], v[34:49]
	v_and_or_b32 v82, v82, s16, 16
	v_and_or_b32 v83, v83, s16, 17
	v_and_or_b32 v84, v84, s16, 18
	v_and_or_b32 v85, v85, s16, 19
	v_med3_f32 v211, v212, v82, v83
	v_and_or_b32 v86, v86, s16, 20
	v_min3_f32 v210, v212, v82, v83
	v_and_or_b32 v87, v87, s16, 21
	v_mfma_f32_32x32x16_f16 v[66:81], v[134:137], v[198:201], v[66:81]
	v_med3_f32 v214, v210, v84, v85
	v_and_or_b32 v88, v88, s16, 22
	v_min3_f32 v212, v210, v84, v85
	v_and_or_b32 v89, v89, s16, 23
	v_min3_f32 v213, v213, v211, v214
	v_med3_f32 v211, v212, v86, v87
	v_and_or_b32 v90, v90, s16, 24
	v_min3_f32 v210, v212, v86, v87
	v_mfma_f32_32x32x16_f16 v[66:81], v[138:141], v[202:205], v[66:81]
	v_and_or_b32 v91, v91, s16, 25
	v_med3_f32 v214, v210, v88, v89
	v_and_or_b32 v92, v92, s16, 26
	v_min3_f32 v212, v210, v88, v89
	v_and_or_b32 v93, v93, s16, 27
	v_min3_f32 v213, v213, v211, v214
	v_med3_f32 v211, v212, v90, v91
	v_and_or_b32 v94, v94, s16, 28
	v_mfma_f32_32x32x16_f16 v[66:81], v[142:145], v[206:209], v[66:81]
	v_min3_f32 v210, v212, v90, v91
	v_and_or_b32 v95, v95, s16, 29
	v_med3_f32 v214, v210, v92, v93
	v_and_or_b32 v96, v96, s16, 30
	v_min3_f32 v212, v210, v92, v93
	v_and_or_b32 v97, v97, s16, 31
	v_min3_f32 v213, v213, v211, v214
	v_med3_f32 v211, v212, v94, v95
	v_min3_f32 v210, v212, v94, v95
	v_med3_f32 v214, v210, v96, v97
	v_min3_f32 v212, v210, v96, v97
	v_min3_f32 v213, v213, v211, v214
	v_mfma_f32_32x32x16_f16 v[82:97], v[146:149], v[194:197], v[50:65]
	v_and_or_b32 v66, v66, s16, 32
	v_and_or_b32 v67, v67, s16, 33
	v_and_or_b32 v68, v68, s16, 34
	v_and_or_b32 v69, v69, s16, 35
	v_med3_f32 v211, v212, v66, v67
	v_and_or_b32 v70, v70, s16, 36
	v_min3_f32 v210, v212, v66, v67
	v_and_or_b32 v71, v71, s16, 37
	v_mfma_f32_32x32x16_f16 v[82:97], v[150:153], v[198:201], v[82:97]
	v_med3_f32 v214, v210, v68, v69
	v_and_or_b32 v72, v72, s16, 38
	v_min3_f32 v212, v210, v68, v69
	v_and_or_b32 v73, v73, s16, 39
	v_min3_f32 v213, v213, v211, v214
	v_med3_f32 v211, v212, v70, v71
	v_and_or_b32 v74, v74, s16, 40
	v_min3_f32 v210, v212, v70, v71
	v_mfma_f32_32x32x16_f16 v[82:97], v[154:157], v[202:205], v[82:97]
	v_and_or_b32 v75, v75, s16, 41
	v_med3_f32 v214, v210, v72, v73
	v_and_or_b32 v76, v76, s16, 42
	v_min3_f32 v212, v210, v72, v73
	v_and_or_b32 v77, v77, s16, 43
	v_min3_f32 v213, v213, v211, v214
	v_med3_f32 v211, v212, v74, v75
	v_and_or_b32 v78, v78, s16, 44
	v_mfma_f32_32x32x16_f16 v[82:97], v[158:161], v[206:209], v[82:97]
	v_min3_f32 v210, v212, v74, v75
	v_and_or_b32 v79, v79, s16, 45
	v_med3_f32 v214, v210, v76, v77
	v_and_or_b32 v80, v80, s16, 46
	v_min3_f32 v212, v210, v76, v77
	v_and_or_b32 v81, v81, s16, 47
	v_min3_f32 v213, v213, v211, v214
	v_med3_f32 v211, v212, v78, v79
	v_min3_f32 v210, v212, v78, v79
	v_med3_f32 v214, v210, v80, v81
	v_min3_f32 v212, v210, v80, v81
	v_min3_f32 v213, v213, v211, v214
	v_and_or_b32 v82, v82, s16, 48
	v_and_or_b32 v83, v83, s16, 49
	v_and_or_b32 v84, v84, s16, 50
	v_and_or_b32 v85, v85, s16, 51
	v_med3_f32 v211, v212, v82, v83
	v_and_or_b32 v86, v86, s16, 52
	v_min3_f32 v210, v212, v82, v83
	v_and_or_b32 v87, v87, s16, 53
	v_med3_f32 v214, v210, v84, v85
	v_and_or_b32 v88, v88, s16, 54
	v_min3_f32 v212, v210, v84, v85
	v_and_or_b32 v89, v89, s16, 55
	v_min3_f32 v213, v213, v211, v214
	v_med3_f32 v211, v212, v86, v87
	v_and_or_b32 v90, v90, s16, 56
	v_min3_f32 v210, v212, v86, v87
	v_and_or_b32 v91, v91, s16, 57
	v_med3_f32 v214, v210, v88, v89
	v_and_or_b32 v92, v92, s16, 58
	v_min3_f32 v212, v210, v88, v89
	v_and_or_b32 v93, v93, s16, 59
	v_min3_f32 v213, v213, v211, v214
	v_med3_f32 v211, v212, v90, v91
	v_and_or_b32 v94, v94, s16, 60
	v_min3_f32 v210, v212, v90, v91
	v_and_or_b32 v95, v95, s16, 61
	v_med3_f32 v214, v210, v92, v93
	v_and_or_b32 v96, v96, s16, 62
	v_min3_f32 v212, v210, v92, v93
	v_or_b32_e32 v97, 63, v97
	v_min3_f32 v213, v213, v211, v214
	v_med3_f32 v211, v212, v94, v95
	v_min3_f32 v210, v212, v94, v95
	v_med3_f32 v214, v210, v96, v97
	v_min3_f32 v212, v210, v96, v97
	v_min3_f32 v213, v213, v211, v214
	s_and_b32 s0, s17, 1
	s_mulk_i32 s0, 0x1200
	v_add_u32_e32 v254, s0, v177
	ds_write_b64 v254, v[212:213]
	v_add_u32_e32 v254, s0, v185
	v_add_u32_e32 v179, 0x1200, v179
	v_add_u32_e32 v188, 0x80, v188
	v_add_u32_e32 v186, 0x80, v186
	v_add_u32_e32 v166, 32, v166
	s_add_i32 s17, s17, 1
	s_cmp_lg_u32 s17, 16
	s_waitcnt lgkmcnt(0)
	s_barrier
	s_cbranch_scc1 .LBB0_88
